# BEST + non-temporal hint on the pooled down-weight conversion stores (P7) and the P0 fp8 W_out / S5 matrix stores
# baseline (speedup 1.0000x reference)
; __device__ __forceinline__ unsigned cvt_pk_bf16(float lo, float hi) { const f32x2 v = {lo, hi}; return __builtin_bit_cast(unsigned, __builtin_convertvector(v, bf16x2_t)); }
; __device__ __forceinline__ void p0_ssm_mats(const Params& P, LAS unsigned char* lds, int tid, int item) {
;     ...
;     bf16_t* Ms = (bf16_t*)(P.ws + WS_SSMM) + (size_t)g * 131072;
;     bf16_t* TM = Ms + 32768;
;     for (int o = tid; o < 32 * 32; o += NTHREADS) {
;         const int row = 32 * q + (o >> 5), c8 = (o & 31) * 8;
;         const int p = row >> 1, j = c8 >> 4, hi0 = c8 & 15;
;         const f32x2 a = pw[(15 - j) * 64 + p];
;         float v[8];
; #pragma unroll
;         for (int k = 0; k < 8; ++k) { const f32x2 bb = Bb[p * 16 + hi0 + k]; v[k] = (row & 1) ? (a.x * bb.y + a.y * bb.x) : (a.x * bb.x - a.y * bb.y); }
;         u32x4 w; w.x = cvt_pk_bf16(v[0], v[1]); w.y = cvt_pk_bf16(v[2], v[3]); w.z = cvt_pk_bf16(v[4], v[5]); w.w = cvt_pk_bf16(v[6], v[7]);
;         *(u32x4*)(Ms + (size_t)row * 256 + c8) = w;
;     }
.LBB0_35:
	s_movk_i32 s26, 0x3c0
	v_ashrrev_i32_e32 v7, 1, v2
	v_and_b32_e32 v8, 8, v4
	v_ashrrev_i32_e32 v3, 31, v2
	v_bitop3_b32 v16, v5, s26, v5 bitop3:0xc
	v_lshlrev_b32_e32 v18, 3, v7
	v_lshlrev_b32_e32 v7, 7, v7
	v_lshlrev_b32_e32 v19, 3, v8
	v_lshlrev_b64 v[8:9], 9, v[2:3]
	v_lshlrev_b32_e32 v3, 3, v16
	v_add3_u32 v7, 0, v7, v19
	v_add3_u32 v3, 0, v3, v18
	ds_read_b128 v[18:21], v7 offset:8720
	ds_read_b128 v[22:25], v7 offset:8736
	ds_read_b128 v[26:29], v7 offset:8752
	ds_read_b64 v[30:31], v3
	ds_read_b128 v[46:49], v7 offset:8704
	s_movk_i32 s30, 0x1ff
	s_waitcnt lgkmcnt(4)
	v_pk_mov_b32 v[52:53], v[18:19], v[20:21] op_sel:[1,0]
	v_mov_b32_e32 v55, v20
	v_mov_b32_e32 v20, v19
	s_waitcnt lgkmcnt(3)
	v_pk_mov_b32 v[56:57], v[22:23], v[24:25] op_sel:[1,0]
	v_mov_b32_e32 v59, v24
	v_mov_b32_e32 v24, v23
	s_waitcnt lgkmcnt(2)
	v_pk_mov_b32 v[60:61], v[26:27], v[28:29] op_sel:[1,0]
	v_mov_b32_e32 v63, v28
	v_mov_b32_e32 v28, v27
	s_waitcnt lgkmcnt(0)
	v_pk_mov_b32 v[64:65], v[46:47], v[48:49] op_sel:[1,0]
	v_mov_b32_e32 v69, v48
	v_mov_b32_e32 v48, v47
	v_and_b32_e32 v13, 32, v6
	v_and_b32_e32 v10, 0xf8, v4
	v_cmp_lt_u32_e32 vcc, s30, v6
	v_mov_b32_e32 v50, v18
	v_mov_b32_e32 v51, v21
	v_mov_b32_e32 v54, v18
	v_mov_b32_e32 v18, v22
	v_mov_b32_e32 v19, v25
	v_mov_b32_e32 v58, v22
	v_mov_b32_e32 v22, v26
	v_mov_b32_e32 v23, v29
	v_mov_b32_e32 v62, v26
	v_mov_b32_e32 v26, v46
	v_mov_b32_e32 v27, v49
	v_mov_b32_e32 v68, v46
	v_pk_mul_f32 v[46:47], v[30:31], v[52:53]
	v_pk_mul_f32 v[20:21], v[30:31], v[20:21] op_sel:[1,0]
	v_pk_mul_f32 v[52:53], v[30:31], v[56:57]
	v_pk_mul_f32 v[24:25], v[30:31], v[24:25] op_sel:[1,0]
	v_pk_mul_f32 v[56:57], v[30:31], v[60:61]
	v_pk_mul_f32 v[28:29], v[30:31], v[28:29] op_sel:[1,0]
	v_pk_mul_f32 v[60:61], v[30:31], v[64:65]
	v_pk_mul_f32 v[48:49], v[30:31], v[48:49] op_sel:[1,0]
	v_add_u32_e32 v14, 0x200, v6
	v_lshlrev_b32_e32 v10, 1, v10
	s_or_b64 s[28:29], vcc, s[28:29]
	v_lshl_add_u64 v[8:9], s[0:1], 0, v[8:9]
	v_pk_fma_f32 v[46:47], v[30:31], v[50:51], v[46:47] op_sel:[1,0,0] op_sel_hi:[0,1,1]
	v_pk_fma_f32 v[20:21], v[30:31], v[54:55], v[20:21] op_sel_hi:[0,1,1] neg_lo:[0,0,1] neg_hi:[0,0,1]
	v_pk_fma_f32 v[18:19], v[30:31], v[18:19], v[52:53] op_sel:[1,0,0] op_sel_hi:[0,1,1]
	v_pk_fma_f32 v[24:25], v[30:31], v[58:59], v[24:25] op_sel_hi:[0,1,1] neg_lo:[0,0,1] neg_hi:[0,0,1]
	v_pk_fma_f32 v[22:23], v[30:31], v[22:23], v[56:57] op_sel:[1,0,0] op_sel_hi:[0,1,1]
	v_pk_fma_f32 v[28:29], v[30:31], v[62:63], v[28:29] op_sel_hi:[0,1,1] neg_lo:[0,0,1] neg_hi:[0,0,1]
	v_pk_fma_f32 v[26:27], v[30:31], v[26:27], v[60:61] op_sel:[1,0,0] op_sel_hi:[0,1,1]
	v_pk_fma_f32 v[30:31], v[30:31], v[68:69], v[48:49] op_sel_hi:[0,1,1] neg_lo:[0,0,1] neg_hi:[0,0,1]
	v_cmp_eq_u32_e32 vcc, 0, v13
	v_mov_b32_e32 v6, v14
	v_lshl_add_u64 v[8:9], v[8:9], 0, v[10:11]
	v_cndmask_b32_e32 v3, v27, v31, vcc
	v_cndmask_b32_e32 v7, v26, v30, vcc
	v_cndmask_b32_e32 v10, v47, v21, vcc
	v_cndmask_b32_e32 v13, v46, v20, vcc
	v_cndmask_b32_e32 v14, v19, v25, vcc
	v_cndmask_b32_e32 v16, v18, v24, vcc
	v_cndmask_b32_e32 v21, v23, v29, vcc
	v_cndmask_b32_e32 v22, v22, v28, vcc
	v_add_u32_e32 v4, 0x1000, v4
	v_add_u32_e32 v5, 0x4000, v5
	v_add_u32_e32 v2, 16, v2
	v_cvt_pk_bf16_f32 v18, v7, v3
	v_cvt_pk_bf16_f32 v19, v13, v10
	v_cvt_pk_bf16_f32 v20, v16, v14
	v_cvt_pk_bf16_f32 v21, v22, v21
	global_store_dwordx4 v[8:9], v[18:21], off nt
	s_andn2_b64 exec, exec, s[28:29]
	s_cbranch_execnz .LBB0_35
	s_or_b64 exec, exec, s[28:29]
	s_add_u32 s0, s0, 0x10000
	s_addc_u32 s1, s1, 0
	s_and_b32 s26, s43, 0xffffffc0
	s_mov_b64 s[28:29], 0
	v_mov_b32_e32 v13, v0
	s_branch .LBB0_39

; #define LAS __attribute__((address_space(3)))
; __device__ __forceinline__ unsigned cvt_pk_bf16(float lo, float hi) { const f32x2 v = {lo, hi}; return __builtin_bit_cast(unsigned, __builtin_convertvector(v, bf16x2_t)); }
; __device__ __forceinline__ void p0_ssm_mats(const Params& P, LAS unsigned char* lds, int tid, int item) {
;     ...
;     for (int o = tid; o < 64 * 48; o += NTHREADS) {
;         const int row = 64 * q + o / 48, c8 = (o % 48) * 8;
;         const int i = row >> 4, ho = row & 15; float v[8];
;         if (c8 < 256) { const int j = c8 >> 4, hi0 = c8 & 15;
;             if (j <= i) { const LAS f32x4* kp = (const LAS f32x4*)(Kt + ((i - j) * 16 + ho) * 16 + hi0); const f32x4 k0 = kp[0], k1 = kp[1];
;                 v[0] = k0[0]; v[1] = k0[1]; v[2] = k0[2]; v[3] = k0[3]; v[4] = k1[0]; v[5] = k1[1]; v[6] = k1[2]; v[7] = k1[3]; }
;             else {
; #pragma unroll
;                 for (int k = 0; k < 8; ++k) v[k] = 0.f; } }
;         else { const int p0 = (c8 - 256) >> 1;
; #pragma unroll
;             for (int k = 0; k < 4; ++k) { const f32x2 c0 = Cc[ho * 65 + p0 + k], a0 = pw[(i + 1) * 64 + p0 + k];
;                 v[2 * k] = c0.x * a0.x - c0.y * a0.y; v[2 * k + 1] = -(c0.x * a0.y + c0.y * a0.x); } }
;         u32x4 w; w.x = cvt_pk_bf16(v[0], v[1]); w.y = cvt_pk_bf16(v[2], v[3]); w.z = cvt_pk_bf16(v[4], v[5]); w.w = cvt_pk_bf16(v[6], v[7]);
;         *(u32x4*)(TM + (size_t)row * 384 + c8) = w;
.LBB0_38:
	s_or_b64 exec, exec, s[30:31]
	s_waitcnt lgkmcnt(1)
	v_cvt_pk_bf16_f32 v2, v2, v3
	v_cvt_pk_bf16_f32 v3, v4, v5
	s_waitcnt lgkmcnt(0)
	v_cvt_pk_bf16_f32 v4, v6, v7
	v_mov_b64_e32 v[6:7], s[0:1]
	v_mad_i64_i32 v[6:7], s[30:31], v10, s41, v[6:7]
	v_lshlrev_b32_e32 v10, 1, v14
	v_cvt_pk_bf16_f32 v5, v8, v9
	v_lshl_add_u64 v[6:7], v[6:7], 0, v[10:11]
	global_store_dwordx4 v[6:7], v[2:5], off nt
	v_cmp_lt_u32_e32 vcc, s42, v13
	s_or_b64 s[28:29], vcc, s[28:29]
	v_add_u32_e32 v2, 0x200, v13
	v_mov_b32_e32 v13, v2
	s_andn2_b64 exec, exec, s[28:29]
	s_cbranch_execz .LBB0_24

; #define LAS __attribute__((address_space(3)))
; __device__ __forceinline__ void cvt8_to_lds(LAS unsigned* tile, const f32x4 (&r)[8], float sc, int tid) {
;     const int kg = tid >> 5, nq = tid & 31;
;     u32x4 w0, w1;
; #pragma unroll
;     for (int j = 0; j < 4; ++j) {
;         int a = 0, b = 0;
;         a = __builtin_amdgcn_cvt_pk_fp8_f32(r[0][j] * sc, r[1][j] * sc, a, false); a = __builtin_amdgcn_cvt_pk_fp8_f32(r[2][j] * sc, r[3][j] * sc, a, true);
;         b = __builtin_amdgcn_cvt_pk_fp8_f32(r[4][j] * sc, r[5][j] * sc, b, false); b = __builtin_amdgcn_cvt_pk_fp8_f32(r[6][j] * sc, r[7][j] * sc, b, true);
;         w0[j] = (unsigned)a; w1[j] = (unsigned)b;
;     }
;     *(LAS u32x4*)(tile + (2 * kg) * 132 + nq * 4) = w0;
;     *(LAS u32x4*)(tile + (2 * kg + 1) * 132 + nq * 4) = w1;
; }
; __device__ __forceinline__ void cvt8_store(const LAS unsigned* tile, const Cvt8Unit& u, int tid) {
;     const int nl = tid >> 2, q = tid & 3;
;     u32x4 w0, w1;
;     w0.x = tile[(8 * q + 0) * 132 + nl]; w0.y = tile[(8 * q + 1) * 132 + nl]; w0.z = tile[(8 * q + 2) * 132 + nl]; w0.w = tile[(8 * q + 3) * 132 + nl];
;     w1.x = tile[(8 * q + 4) * 132 + nl]; w1.y = tile[(8 * q + 5) * 132 + nl]; w1.z = tile[(8 * q + 6) * 132 + nl]; w1.w = tile[(8 * q + 7) * 132 + nl];
;     const int n = u.n0 + nl;
;     int np = n;
;     if (u.nmode == 1 || u.nmode == 2) np = (n >> 7) * 256 + (n & 127) + (u.nmode == 2 ? 128 : 0);
;     unsigned char* d = u.dst + (size_t)(np >> 8) * ((size_t)u.Kd * 256) + (size_t)(u.k0 >> 7) * 32768 + (np & 255) * 128 + q * 32;
;     *(u32x4*)d = w0; *(u32x4*)(d + 16) = w1;
; }
; __device__ __forceinline__ void p0_convert_wout_fp8(const Params& P, LAS unsigned char* lds, int tid, int blk, int G, const f32x4 (&pre)[8]) {
;     ...
;     for (int L = blk; L < 256; L += G) {
;         Cvt8Unit u; p0_wout_unit(P, L, u);
;         f32x4 r[8];
;         if (L == blk) {
; #pragma unroll
;             for (int i = 0; i < 8; ++i) r[i] = pre[i];
;         } else cvt8_load(u, tid, r);
;         const int kb = u.k0 + 8 * (tid >> 5);
; #pragma unroll
;         for (int kk = 0; kk < 8; ++kk) { const int k = kb + kk; r[kk] *= (k < 1024) ? P.in[15][k] : P.in[16][k - 1024]; }
;         cvt8_to_lds(tile, r, u.scale, tid);
;         __syncthreads();
;         cvt8_store(tile, u, tid);
;         __syncthreads();
;     }
.LBB0_140:
	v_readlane_b32 s52, v254, 23
	v_lshlrev_b64 v[78:79], 2, v[72:73]
	v_readlane_b32 s66, v254, 37
	v_readlane_b32 s67, v254, 38
	v_cmp_gt_i32_e32 vcc, s39, v72
	s_add_i32 s0, s2, s47
	v_lshl_add_u64 v[80:81], s[66:67], 0, v[78:79]
	v_lshl_add_u64 v[78:79], s[80:81], 0, v[78:79]
	v_lshl_add_u64 v[82:83], v[78:79], 0, s[6:7]
	v_cndmask_b32_e32 v83, v83, v81, vcc
	v_cndmask_b32_e32 v82, v82, v80, vcc
	global_load_dword v70, v[82:83], off
	v_lshl_add_u64 v[82:83], v[80:81], 0, 4
	v_lshl_add_u64 v[84:85], v[78:79], 0, s[8:9]
	v_cmp_gt_i32_e32 vcc, s40, v72
	v_lshl_add_u64 v[86:87], v[78:79], 0, s[10:11]
	v_lshl_add_u64 v[88:89], v[78:79], 0, s[24:25]
	v_cndmask_b32_e32 v83, v85, v83, vcc
	v_cndmask_b32_e32 v82, v84, v82, vcc
	global_load_dword v84, v[82:83], off
	v_lshl_add_u64 v[82:83], v[80:81], 0, 8
	v_cmp_gt_i32_e32 vcc, s41, v72
	v_lshl_add_u64 v[90:91], v[78:79], 0, s[26:27]
	v_lshl_add_u64 v[92:93], v[78:79], 0, s[28:29]
	v_cndmask_b32_e32 v83, v87, v83, vcc
	v_cndmask_b32_e32 v82, v86, v82, vcc
	global_load_dword v86, v[82:83], off
	v_lshl_add_u64 v[82:83], v[80:81], 0, 12
	v_cmp_gt_i32_e32 vcc, s42, v72
	v_lshl_add_u64 v[94:95], v[78:79], 0, s[30:31]
	v_lshl_add_u64 v[78:79], v[78:79], 0, s[34:35]
	v_cndmask_b32_e32 v83, v89, v83, vcc
	v_cndmask_b32_e32 v82, v88, v82, vcc
	global_load_dword v88, v[82:83], off
	v_lshl_add_u64 v[82:83], v[80:81], 0, 16
	v_cmp_gt_i32_e32 vcc, s43, v72
	s_add_i32 s47, s47, s33
	s_add_i32 s36, s36, s37
	v_cndmask_b32_e32 v83, v91, v83, vcc
	v_cndmask_b32_e32 v82, v90, v82, vcc
	global_load_dword v90, v[82:83], off
	v_lshl_add_u64 v[82:83], v[80:81], 0, 20
	v_cmp_gt_i32_e32 vcc, s44, v72
	s_add_i32 s3, s3, s38
	v_readlane_b32 s53, v254, 24
	v_cndmask_b32_e32 v83, v93, v83, vcc
	v_cndmask_b32_e32 v82, v92, v82, vcc
	global_load_dword v92, v[82:83], off
	v_lshl_add_u64 v[82:83], v[80:81], 0, 24
	v_cmp_gt_i32_e32 vcc, s45, v72
	v_lshl_add_u64 v[80:81], v[80:81], 0, 28
	v_readlane_b32 s54, v254, 25
	v_cndmask_b32_e32 v83, v95, v83, vcc
	v_cndmask_b32_e32 v82, v94, v82, vcc
	v_cmp_gt_i32_e32 vcc, s46, v72
	global_load_dword v94, v[82:83], off
	v_mov_b32_e32 v83, 0
	v_cndmask_b32_e32 v73, v79, v81, vcc
	v_cndmask_b32_e32 v72, v78, v80, vcc
	global_load_dword v72, v[72:73], off
	v_mov_b32_e32 v78, 0
	v_mov_b32_e32 v79, 0
	v_mov_b32_e32 v80, 0
	v_mov_b32_e32 v81, 0
	v_mov_b32_e32 v82, 0
	v_readlane_b32 s55, v254, 26
	v_readlane_b32 s56, v254, 27
	v_readlane_b32 s57, v254, 28
	v_readlane_b32 s58, v254, 29
	v_readlane_b32 s59, v254, 30
	v_readlane_b32 s60, v254, 31
	v_readlane_b32 s61, v254, 32
	v_readlane_b32 s62, v254, 33
	v_readlane_b32 s63, v254, 34
	v_readlane_b32 s64, v254, 35
	v_readlane_b32 s65, v254, 36
	s_waitcnt vmcnt(7)
	v_pk_mul_f32 v[30:31], v[30:31], v[70:71] op_sel_hi:[1,0]
	s_nop 0
	v_mul_f32_e32 v30, 0x42800000, v30
	v_mul_f32_e32 v31, 0x42800000, v31
	v_pk_mul_f32 v[32:33], v[32:33], v[70:71] op_sel_hi:[1,0]
	s_waitcnt vmcnt(6)
	v_pk_mul_f32 v[34:35], v[34:35], v[84:85] op_sel_hi:[1,0]
	s_nop 0
	v_mul_f32_e32 v34, 0x42800000, v34
	v_mul_f32_e32 v35, 0x42800000, v35
	v_pk_mul_f32 v[36:37], v[36:37], v[84:85] op_sel_hi:[1,0]
	v_cvt_pk_fp8_f32 v78, v30, v34
	v_cvt_pk_fp8_f32 v79, v31, v35
	v_mov_b32_e32 v84, 0
	s_waitcnt vmcnt(5)
	v_pk_mul_f32 v[40:41], v[40:41], v[86:87] op_sel_hi:[1,0]
	v_mov_b32_e32 v85, 0
	v_pk_mul_f32 v[38:39], v[38:39], v[86:87] op_sel_hi:[1,0]
	s_waitcnt vmcnt(4)
	v_pk_mul_f32 v[44:45], v[44:45], v[88:89] op_sel_hi:[1,0]
	v_pk_mul_f32 v[42:43], v[42:43], v[88:89] op_sel_hi:[1,0]
	v_mul_f32_e32 v38, 0x42800000, v38
	v_mul_f32_e32 v42, 0x42800000, v42
	v_mul_f32_e32 v39, 0x42800000, v39
	v_mul_f32_e32 v43, 0x42800000, v43
	v_cvt_pk_fp8_f32 v78, v38, v42 op_sel:[0,0,1]
	s_waitcnt vmcnt(3)
	v_pk_mul_f32 v[46:47], v[46:47], v[90:91] op_sel_hi:[1,0]
	v_pk_mul_f32 v[48:49], v[48:49], v[90:91] op_sel_hi:[1,0]
	v_mul_f32_e32 v47, 0x42800000, v47
	v_mul_f32_e32 v46, 0x42800000, v46
	v_cvt_pk_fp8_f32 v79, v39, v43 op_sel:[0,0,1]
	s_waitcnt vmcnt(2)
	v_pk_mul_f32 v[50:51], v[50:51], v[92:93] op_sel_hi:[1,0]
	s_nop 0
	v_mul_f32_e32 v51, 0x42800000, v51
	v_cvt_pk_fp8_f32 v83, v47, v51
	v_pk_mul_f32 v[52:53], v[52:53], v[92:93] op_sel_hi:[1,0]
	v_mul_f32_e32 v50, 0x42800000, v50
	v_mul_f32_e32 v34, 0x42800000, v52
	v_cvt_pk_fp8_f32 v82, v46, v50
	s_waitcnt vmcnt(1)
	v_pk_mul_f32 v[54:55], v[54:55], v[94:95] op_sel_hi:[1,0]
	s_nop 0
	v_mul_f32_e32 v30, 0x42800000, v55
	v_pk_mul_f32 v[56:57], v[56:57], v[94:95] op_sel_hi:[1,0]
	v_mul_f32_e32 v54, 0x42800000, v54
	s_waitcnt vmcnt(0)
	v_pk_mul_f32 v[58:59], v[58:59], v[72:73] op_sel_hi:[1,0]
	v_pk_mul_f32 v[60:61], v[60:61], v[72:73] op_sel_hi:[1,0]
	v_mul_f32_e32 v31, 0x42800000, v59
	v_cvt_pk_fp8_f32 v83, v30, v31 op_sel:[0,0,1]
	v_mul_f32_e32 v30, 0x42800000, v32
	v_mul_f32_e32 v31, 0x42800000, v36
	v_cvt_pk_fp8_f32 v80, v30, v31
	v_mul_f32_e32 v32, 0x42800000, v48
	v_cvt_pk_fp8_f32 v84, v32, v34
	v_mul_f32_e32 v30, 0x42800000, v40
	v_mul_f32_e32 v31, 0x42800000, v44
	v_cvt_pk_fp8_f32 v80, v30, v31 op_sel:[0,0,1]
	v_mul_f32_e32 v30, 0x42800000, v56
	v_mul_f32_e32 v31, 0x42800000, v60
	v_cvt_pk_fp8_f32 v84, v30, v31 op_sel:[0,0,1]
	v_mul_f32_e32 v30, 0x42800000, v33
	v_mul_f32_e32 v31, 0x42800000, v37
	v_cvt_pk_fp8_f32 v81, v30, v31
	v_mul_f32_e32 v32, 0x42800000, v49
	v_mul_f32_e32 v33, 0x42800000, v53
	v_cvt_pk_fp8_f32 v85, v32, v33
	v_mul_f32_e32 v30, 0x42800000, v41
	v_mul_f32_e32 v31, 0x42800000, v45
	v_mul_f32_e32 v58, 0x42800000, v58
	v_cvt_pk_fp8_f32 v81, v30, v31 op_sel:[0,0,1]
	v_mul_f32_e32 v30, 0x42800000, v57
	v_mul_f32_e32 v31, 0x42800000, v61
	v_cvt_pk_fp8_f32 v82, v54, v58 op_sel:[0,0,1]
	v_cvt_pk_fp8_f32 v85, v30, v31 op_sel:[0,0,1]
	v_add_u32_e32 v40, s48, v74
	v_add_u32_e32 v32, 0x400, v77
	v_lshlrev_b32_e32 v38, 11, v40
	s_ashr_i32 s48, s0, 4
	ds_write_b128 v1, v[78:81]
	ds_write_b128 v76, v[82:85]
	s_waitcnt lgkmcnt(0)
	s_barrier
	ds_read2_b32 v[30:31], v77 offset1:132
	ds_read2_b32 v[32:33], v32 offset0:8 offset1:140
	v_add_u32_e32 v34, 0x800, v77
	v_add_u32_e32 v36, 0xc00, v77
	v_and_b32_e32 v70, 0x780000, v38
	s_ashr_i32 s49, s48, 31
	ds_read2_b32 v[34:35], v34 offset0:16 offset1:148
	ds_read2_b32 v[36:37], v36 offset0:24 offset1:156
	v_lshl_add_u64 v[38:39], s[4:5], 0, v[70:71]
	s_lshl_b64 s[48:49], s[48:49], 15
	v_lshlrev_b32_e32 v40, 7, v40
	v_lshl_add_u64 v[38:39], v[38:39], 0, s[48:49]
	v_and_b32_e32 v70, 0x7f80, v40
	v_lshl_add_u64 v[38:39], v[38:39], 0, v[70:71]
	s_add_i32 s0, s2, s47
	v_lshl_add_u64 v[38:39], v[38:39], 0, v[68:69]
	s_cmpk_lt_i32 s0, 0x100
	s_waitcnt lgkmcnt(2)
	global_store_dwordx4 v[38:39], v[30:33], off nt
	s_waitcnt lgkmcnt(0)
	global_store_dwordx4 v[38:39], v[34:37], off offset:16 nt
	s_barrier
	s_cbranch_scc0 .LBB0_143

; #define LAS __attribute__((address_space(3)))
; __device__ __forceinline__ void cvt8_store(const LAS unsigned* tile, const Cvt8Unit& u, int tid) {
;     const int nl = tid >> 2, q = tid & 3;
;     u32x4 w0, w1;
;     w0.x = tile[(8 * q + 0) * 132 + nl]; w0.y = tile[(8 * q + 1) * 132 + nl]; w0.z = tile[(8 * q + 2) * 132 + nl]; w0.w = tile[(8 * q + 3) * 132 + nl];
;     w1.x = tile[(8 * q + 4) * 132 + nl]; w1.y = tile[(8 * q + 5) * 132 + nl]; w1.z = tile[(8 * q + 6) * 132 + nl]; w1.w = tile[(8 * q + 7) * 132 + nl];
;     const int n = u.n0 + nl;
;     int np = n;
;     if (u.nmode == 1 || u.nmode == 2) np = (n >> 7) * 256 + (n & 127) + (u.nmode == 2 ? 128 : 0);
;     unsigned char* d = u.dst + (size_t)(np >> 8) * ((size_t)u.Kd * 256) + (size_t)(u.k0 >> 7) * 32768 + (np & 255) * 128 + q * 32;
;     *(u32x4*)d = w0; *(u32x4*)(d + 16) = w1;
; }
; __device__ __forceinline__ void p0_convert_fp8(const Params& P, LAS unsigned char* lds, int tid, int blk, int G, const int Lbeg, const int Lend) {
;     ...
;         cvt8_store(tileA, uA, tid);
;         if (hasB) cvt8_store(tileB, uB, tid);
.LBB0_1216:
	v_add_u32_e32 v10, s6, v1
	s_add_i32 s6, s11, -1
	s_cmp_lt_u32 s6, 2
	s_cselect_b64 vcc, -1, 0
	v_lshlrev_b32_e32 v11, 1, v10
	s_cmp_eq_u32 s11, 2
	v_and_b32_e32 v11, 0xffffff00, v11
	v_and_b32_e32 v12, 0x7f, v10
	s_cselect_b32 s6, 0x80, 0
	v_or3_b32 v11, v12, s6, v11
	v_cndmask_b32_e32 v12, v10, v11, vcc
	v_ashrrev_i32_e32 v13, 8, v12
	v_ashrrev_i32_e32 v10, 31, v13
	s_lshl_b32 s6, s10, 8
	v_mul_lo_u32 v14, s6, v10
	v_mov_b64_e32 v[10:11], s[0:1]
	s_ashr_i32 s11, s10, 31
	v_mad_u64_u32 v[10:11], s[0:1], s6, v13, v[10:11]
	v_add_u32_e32 v4, 0x400, v139
	v_add_u32_e32 v6, 0x800, v139
	v_add_u32_e32 v8, 0xc00, v139
	s_lshr_b64 s[10:11], s[10:11], 24
	s_ashr_i32 s0, s25, 7
	s_waitcnt lgkmcnt(0)
	s_barrier
	ds_read2_b32 v[2:3], v139 offset1:132
	ds_read2_b32 v[4:5], v4 offset0:8 offset1:140
	ds_read2_b32 v[6:7], v6 offset0:16 offset1:148
	ds_read2_b32 v[8:9], v8 offset0:24 offset1:156
	v_mul_i32_i24_e32 v15, s10, v13
	s_ashr_i32 s1, s0, 31
	v_add3_u32 v11, v15, v11, v14
	s_lshl_b64 s[0:1], s[0:1], 15
	v_lshlrev_b32_e32 v12, 7, v12
	v_lshl_add_u64 v[10:11], v[10:11], 0, s[0:1]
	v_and_b32_e32 v134, 0x7f80, v12
	v_lshl_add_u64 v[10:11], v[10:11], 0, v[134:135]
	v_lshl_add_u64 v[10:11], v[10:11], 0, v[132:133]
	s_and_b64 vcc, exec, s[4:5]
	s_waitcnt lgkmcnt(2)
	global_store_dwordx4 v[10:11], v[2:5], off nt
	s_waitcnt lgkmcnt(0)
	global_store_dwordx4 v[10:11], v[6:9], off offset:16 nt
	s_cbranch_vccnz .LBB0_1218
	s_add_i32 s0, s57, -1
	v_add_u32_e32 v10, s14, v1
	s_cmp_lt_u32 s0, 2
	s_cselect_b64 vcc, -1, 0
	v_lshlrev_b32_e32 v11, 1, v10
	s_cmp_eq_u32 s57, 2
	v_and_b32_e32 v11, 0xffffff00, v11
	v_and_b32_e32 v12, 0x7f, v10
	s_cselect_b32 s0, 0x80, 0
	v_or3_b32 v11, v12, s0, v11
	v_cndmask_b32_e32 v12, v10, v11, vcc
	v_ashrrev_i32_e32 v13, 8, v12
	v_ashrrev_i32_e32 v10, 31, v13
	s_ashr_i32 s25, s24, 31
	s_lshl_b32 s4, s24, 8
	v_mul_lo_u32 v14, s4, v10
	s_lshr_b64 s[0:1], s[24:25], 24
	v_mov_b64_e32 v[10:11], s[12:13]
	v_mul_i32_i24_e32 v15, s0, v13
	v_mad_u64_u32 v[10:11], s[0:1], s4, v13, v[10:11]
	v_add_u32_e32 v2, 0x4200, v139
	v_add_u32_e32 v4, 0x4600, v139
	s_ashr_i32 s0, s56, 7
	ds_read2_b32 v[2:3], v2 offset1:132
	ds_read2_b32 v[4:5], v4 offset0:8 offset1:140
	v_add_u32_e32 v6, 0x4a00, v139
	v_add_u32_e32 v8, 0x4e00, v139
	s_ashr_i32 s1, s0, 31
	ds_read2_b32 v[6:7], v6 offset0:16 offset1:148
	ds_read2_b32 v[8:9], v8 offset0:24 offset1:156
	v_add3_u32 v11, v15, v11, v14
	s_lshl_b64 s[0:1], s[0:1], 15
	v_lshlrev_b32_e32 v12, 7, v12
	v_lshl_add_u64 v[10:11], v[10:11], 0, s[0:1]
	v_and_b32_e32 v134, 0x7f80, v12
	v_lshl_add_u64 v[10:11], v[10:11], 0, v[134:135]
	v_lshl_add_u64 v[10:11], v[10:11], 0, v[132:133]
	s_waitcnt lgkmcnt(2)
	global_store_dwordx4 v[10:11], v[2:5], off nt
	s_waitcnt lgkmcnt(0)
	global_store_dwordx4 v[10:11], v[6:9], off offset:16 nt
